# MoE down GEMM K-loop restructured to 16 fp8 MFMAs per barrier interval (same schedule as the bf16 GEMM phases), prologue reordered to match
# speedup vs baseline: 1.0159x; 1.0142x over previous
;     __device__ bool next(int i, Unit& u) const {
;         const long L = (long)i * G + c; if (L >= nwg) return false;
;         int wgid = (int)L; { const int q = nwg / NXCD, r = nwg % NXCD, xcd = wgid % NXCD, off = wgid / NXCD; wgid = (xcd < r ? xcd * (q + 1) : r * (q + 1) + (xcd - r) * q) + off; }
;         int e = 0;
;         for (int j = 1; j < NEXP; ++j) if (tile0[j] * NC <= wgid) e = j;
;         const int nr = tile0[e + 1] - tile0[e], idx = wgid - tile0[e] * NC;
;         const int r = idx % nr, cn = idx / nr;
;         u.e = __builtin_amdgcn_readfirstlane(e); u.pm = __builtin_amdgcn_readfirstlane(tile0[e] + r); u.pn = __builtin_amdgcn_readfirstlane(e * NC + cn); u.r0 = __builtin_amdgcn_readfirstlane(r * BM); return true;
; template <class Epi, class Sched, bool GATHER, bool ALIGN_EPI, bool SP2, bool FP8>
; __device__ __forceinline__ void gemm_phase(LAS unsigned char* lds, const Gemm g, const Sched& S, const Epi& E) {
;     ...
;     for (int i = 0; i < 2; ++i) { int R, C; stage_rc(tid * 16 + i * 8192, R, C); Rr[i] = R; Cc[i] = C; const int Rb = (R & ~31) + perm32(R & 31); voffB[i] = (unsigned)(Rb * K + C) * 2u; }
;     const int kstep = BK * 2;
;     const int hstep = HALF * K * 2;
;     const int tstep = 2 * hstep;
;     const unsigned ldsw = (unsigned)wid * 1024u;
;     const int aoff = lds_byte(wr * 64 + fr, fq * 8), boff = lds_byte(wc * 32 + fr, fq * 8);
;     const __amdgpu_buffer_rsrc_t rsA = __builtin_amdgcn_make_buffer_rsrc((void*)g.A, 0, 0xFFFFFFF0u, 0x00020000);
;     const __amdgpu_buffer_rsrc_t rsB = __builtin_amdgcn_make_buffer_rsrc((void*)g.Bt, 0, 0xFFFFFFF0u, 0x00020000);
.LBB0_996:
	s_or_b64 exec, exec, s[4:5]
	s_add_i32 s0, 0, 0x27d80
	v_mov_b32_e32 v1, s0
	s_waitcnt vmcnt(0) lgkmcnt(0)
	s_barrier
	ds_read_b32 v1, v1
	v_readlane_b32 s0, v245, 18
	s_waitcnt lgkmcnt(0)
	v_lshlrev_b32_e32 v164, 3, v1
	v_cmp_ge_i32_e32 vcc, s0, v164
	v_readfirstlane_b32 s0, v0
	s_cbranch_vccnz .LBB0_1014
	s_add_u32 s4, s96, 0x3d800000
	s_addc_u32 s5, s97, 0
	v_lshlrev_b32_e32 v2, 4, v0
	v_and_b32_e32 v3, 32, v0
	s_add_u32 s8, s96, 0x21000000
	v_bitop3_b32 v2, v2, v3, 48 bitop3:0x6c
	v_readlane_b32 s13, v245, 18
	s_addc_u32 s9, s97, 0
	v_and_or_b32 v3, v0, 64, v2
	v_lshrrev_b32_e32 v2, 1, v0
	v_lshrrev_b32_e32 v4, 5, v0
	s_ashr_i32 s19, s13, 31
	v_and_b32_e32 v2, 24, v2
	v_and_b32_e32 v4, 4, v4
	v_bfe_u32 v5, v0, 2, 2
	s_lshr_b32 s10, s19, 29
	v_or3_b32 v4, v4, v5, v2
	v_lshrrev_b32_e32 v12, 3, v0
	s_add_i32 s10, s13, s10
	s_lshr_b32 s1, s0, 6
	v_and_or_b32 v5, v12, 32, v4
	s_ashr_i32 s11, s10, 3
	s_and_b32 s10, s10, -8
	v_lshl_or_b32 v163, v5, 11, v3
	v_bfe_u32 v5, v0, 3, 25
	s_lshr_b32 s16, s0, 8
	s_lshl_b32 s12, s1, 10
	s_and_b32 s5, s5, 0xffff
	s_and_b32 s9, s9, 0xffff
	s_sub_i32 s10, s13, s10
	v_or_b32_e32 v13, 64, v5
	s_movk_i32 s6, 0x60
	s_cmp_lt_i32 s10, 0
	v_and_or_b32 v4, v13, s6, v4
	v_add_u32_e32 v169, 1, v1
	s_cselect_b64 vcc, -1, 0
	v_lshl_or_b32 v168, v4, 11, v3
	v_cndmask_b32_e32 v4, v1, v169, vcc
	v_mul_lo_u32 v4, v4, s10
	s_add_i32 s10, 0, 0x27d04
	v_add_u32_e32 v14, s11, v4
	v_mov_b32_e32 v4, s10
	ds_read2_b32 v[4:5], v4 offset1:1
	s_add_i32 s10, 0, 0x27d0c
	v_mov_b32_e32 v6, s10
	s_add_i32 s10, 0, 0x27d14
	v_mov_b32_e32 v8, s10
	s_add_i32 s10, 0, 0x27d1c
	v_mov_b32_e32 v10, s10
	ds_read2_b32 v[6:7], v6 offset1:1
	ds_read2_b32 v[8:9], v8 offset1:1
	ds_read2_b32 v[10:11], v10 offset1:1
	s_waitcnt lgkmcnt(3)
	v_lshlrev_b32_e32 v4, 3, v4
	v_cmp_le_i32_e32 vcc, v4, v14
	v_lshlrev_b32_e32 v5, 3, v5
	s_add_i32 s10, 0, 0x27d24
	v_cndmask_b32_e64 v4, 0, 1, vcc
	v_cmp_gt_i32_e32 vcc, v5, v14
	s_waitcnt lgkmcnt(2)
	v_lshlrev_b32_e32 v5, 3, v6
	s_movk_i32 s13, 0x70
	v_cndmask_b32_e32 v4, 2, v4, vcc
	v_cmp_gt_i32_e32 vcc, v5, v14
	v_lshlrev_b32_e32 v5, 3, v7
	s_add_i32 s20, s12, 0
	v_cndmask_b32_e32 v4, 3, v4, vcc
	v_cmp_gt_i32_e32 vcc, v5, v14
	s_waitcnt lgkmcnt(1)
	v_lshlrev_b32_e32 v5, 3, v8
	s_mov_b32 s7, 0x20000
	v_cndmask_b32_e32 v4, 4, v4, vcc
	v_cmp_gt_i32_e32 vcc, v5, v14
	v_lshlrev_b32_e32 v5, 3, v9
	s_mov_b32 s6, -16
	v_cndmask_b32_e32 v4, 5, v4, vcc
	v_cmp_gt_i32_e32 vcc, v5, v14
	s_waitcnt lgkmcnt(0)
	v_lshlrev_b32_e32 v5, 3, v10
	s_add_i32 s21, s20, 0x10000
	v_cndmask_b32_e32 v4, 6, v4, vcc
	v_cmp_gt_i32_e32 vcc, v5, v14
	v_lshlrev_b32_e32 v5, 3, v11
	s_mov_b32 s11, s7
	v_cndmask_b32_e32 v4, 7, v4, vcc
	v_cmp_gt_i32_e32 vcc, v5, v14
	s_mov_b32 m0, s21
	s_add_i32 s22, s20, 0x12000
	v_cndmask_b32_e32 v15, 8, v4, vcc
	v_mov_b32_e32 v4, s10
	ds_read2_b32 v[4:5], v4 offset1:1
	s_add_i32 s10, 0, 0x27d2c
	v_mov_b32_e32 v6, s10
	s_add_i32 s10, 0, 0x27d34
	v_mov_b32_e32 v8, s10
	s_add_i32 s10, 0, 0x27d3c
	v_mov_b32_e32 v10, s10
	ds_read2_b32 v[6:7], v6 offset1:1
	ds_read2_b32 v[8:9], v8 offset1:1
	ds_read2_b32 v[10:11], v10 offset1:1
	s_waitcnt lgkmcnt(3)
	v_lshlrev_b32_e32 v4, 3, v4
	v_cmp_gt_i32_e32 vcc, v4, v14
	v_lshlrev_b32_e32 v5, 3, v5
	s_add_i32 s10, 0, 0x27d44
	v_cndmask_b32_e32 v4, 9, v15, vcc
	v_cmp_gt_i32_e32 vcc, v5, v14
	s_waitcnt lgkmcnt(2)
	v_lshlrev_b32_e32 v5, 3, v6
	s_add_i32 s23, s20, 0x2000
	v_cndmask_b32_e32 v4, 10, v4, vcc
	v_cmp_gt_i32_e32 vcc, v5, v14
	v_lshlrev_b32_e32 v5, 3, v7
	s_add_i32 s24, s20, 0x14000
	v_cndmask_b32_e32 v4, 11, v4, vcc
	v_cmp_gt_i32_e32 vcc, v5, v14
	s_waitcnt lgkmcnt(1)
	v_lshlrev_b32_e32 v5, 3, v8
	s_add_i32 s25, s20, 0x16000
	v_cndmask_b32_e32 v4, 12, v4, vcc
	v_cmp_gt_i32_e32 vcc, v5, v14
	v_lshlrev_b32_e32 v5, 3, v9
	s_add_i32 s26, s20, 0x4000
	v_cndmask_b32_e32 v4, 13, v4, vcc
	v_cmp_gt_i32_e32 vcc, v5, v14
	s_waitcnt lgkmcnt(0)
	v_lshlrev_b32_e32 v5, 3, v10
	s_add_i32 s27, s20, 0x6000
	v_cndmask_b32_e32 v4, 14, v4, vcc
	v_cmp_gt_i32_e32 vcc, v5, v14
	v_lshlrev_b32_e32 v5, 3, v11
	s_nop 0
	v_cndmask_b32_e32 v4, 15, v4, vcc
	v_cmp_gt_i32_e32 vcc, v5, v14
	s_nop 1
	v_cndmask_b32_e32 v15, 16, v4, vcc
	v_mov_b32_e32 v4, s10
	ds_read2_b32 v[4:5], v4 offset1:1
	s_add_i32 s10, 0, 0x27d4c
	v_mov_b32_e32 v6, s10
	s_add_i32 s10, 0, 0x27d54
	v_mov_b32_e32 v8, s10
	s_add_i32 s10, 0, 0x27d5c
	v_mov_b32_e32 v10, s10
	ds_read2_b32 v[6:7], v6 offset1:1
	ds_read2_b32 v[8:9], v8 offset1:1
	ds_read2_b32 v[10:11], v10 offset1:1
	s_waitcnt lgkmcnt(3)
	v_lshlrev_b32_e32 v4, 3, v4
	v_cmp_gt_i32_e32 vcc, v4, v14
	v_lshlrev_b32_e32 v5, 3, v5
	s_add_i32 s10, 0, 0x27d64
	v_cndmask_b32_e32 v4, 17, v15, vcc
	v_cmp_gt_i32_e32 vcc, v5, v14
	s_waitcnt lgkmcnt(2)
	v_lshlrev_b32_e32 v5, 3, v6
	v_cndmask_b32_e32 v4, 18, v4, vcc
	v_cmp_gt_i32_e32 vcc, v5, v14
	v_lshlrev_b32_e32 v5, 3, v7
	s_nop 0
	v_cndmask_b32_e32 v4, 19, v4, vcc
	v_cmp_gt_i32_e32 vcc, v5, v14
	s_waitcnt lgkmcnt(1)
	v_lshlrev_b32_e32 v5, 3, v8
	v_cndmask_b32_e32 v4, 20, v4, vcc
	v_cmp_gt_i32_e32 vcc, v5, v14
	v_lshlrev_b32_e32 v5, 3, v9
	s_nop 0
	v_cndmask_b32_e32 v4, 21, v4, vcc
	v_cmp_gt_i32_e32 vcc, v5, v14
	s_waitcnt lgkmcnt(0)
	v_lshlrev_b32_e32 v5, 3, v10
	v_cndmask_b32_e32 v4, 22, v4, vcc
	v_cmp_gt_i32_e32 vcc, v5, v14
	v_lshlrev_b32_e32 v5, 3, v11
	s_nop 0
	v_cndmask_b32_e32 v4, 23, v4, vcc
	v_cmp_gt_i32_e32 vcc, v5, v14
	s_nop 1
	v_cndmask_b32_e32 v10, 24, v4, vcc
	v_mov_b32_e32 v4, s10
	ds_read2_b32 v[4:5], v4 offset1:1
	s_add_i32 s10, 0, 0x27d6c
	v_mov_b32_e32 v6, s10
	s_add_i32 s10, 0, 0x27d74
	v_mov_b32_e32 v8, s10
	s_add_i32 s10, 0, 0x27d7c
	v_mov_b32_e32 v11, s10
	ds_read2_b32 v[6:7], v6 offset1:1
	ds_read2_b32 v[8:9], v8 offset1:1
	ds_read_b32 v11, v11
	s_waitcnt lgkmcnt(3)
; #define PG8_SETA(d0, d1, u) do { d0.x = PG8_OFFA(u, Rr[0], 0); d0.y = PG8_OFFA(u, Rr[1], 1); d1.x = PG8_OFFA(u, HALF + Rr[0], 0); d1.y = PG8_OFFA(u, HALF + Rr[1], 1); } while (0)
; #define PG8_STAGE_A(bufoff, soff, voff) do { _Pragma("unroll") for (int _i = 0; _i < 2; ++_i) \
;         __builtin_amdgcn_raw_ptr_buffer_load_lds(rsA, (LAS void*)(lds + (bufoff) + ldsw + _i * 8192), 16, (voff)[_i], (soff), 0, 0); } while (0)
; #define PG8_STAGE_B(bufoff, soff) do { _Pragma("unroll") for (int _i = 0; _i < 2; ++_i) \
;         __builtin_amdgcn_raw_ptr_buffer_load_lds(rsB, (LAS void*)(lds + (bufoff) + ldsw + _i * 8192), 16, voffB[_i], (soff), 0, 0); } while (0)
; #define PG8_WAIT_V(n) asm volatile("s_waitcnt vmcnt(" #n ")" ::: "memory")
; #define PG8_BAR __builtin_amdgcn_s_barrier()
;     __device__ bool next(int i, Unit& u) const {
;     ...
;         int wgid = (int)L; { const int q = nwg / NXCD, r = nwg % NXCD, xcd = wgid % NXCD, off = wgid / NXCD; wgid = (xcd < r ? xcd * (q + 1) : r * (q + 1) + (xcd - r) * q) + off; }
;         int e = 0;
;         for (int j = 1; j < NEXP; ++j) if (tile0[j] * NC <= wgid) e = j;
;         const int nr = tile0[e + 1] - tile0[e], idx = wgid - tile0[e] * NC;
;         const int r = idx % nr, cn = idx / nr;
;         u.e = __builtin_amdgcn_readfirstlane(e); u.pm = __builtin_amdgcn_readfirstlane(tile0[e] + r); u.pn = __builtin_amdgcn_readfirstlane(e * NC + cn); u.r0 = __builtin_amdgcn_readfirstlane(r * BM); return true;
; template <class Epi, class Sched, bool GATHER, bool ALIGN_EPI, bool SP2, bool FP8>
; __device__ __forceinline__ void gemm_phase(LAS unsigned char* lds, const Gemm g, const Sched& S, const Epi& E) {
;     ...
;     int cA = GATHER ? 0 : cur.pm * tstep, cB = cur.pn * tstep;
;     PG8_SETA(vA0, vA1, cur);
;     if constexpr (SP2) {
;         PG8_STAGE_B(PG8_SB(0, 0), cB); PG8_STAGE_B(PG8_SB(0, 1), cB + hstep); PG8_STAGE_A(PG8_SA(0, 0), cA, vA0); PG8_STAGE_A(PG8_SA(0, 1), cA, vA1);
;         if (wr == 1) PG8_BAR;
;         PG8_WAIT_V(2); PG8_BAR;
;         PG8_STAGE_B(PG8_SB(1, 0), cB + kstep); PG8_STAGE_A(PG8_SA(1, 0), cA + kstep, vA0); PG8_STAGE_B(PG8_SB(1, 1), cB + hstep + kstep);
;         PG8_WAIT_V(6); PG8_BAR;
;     } else {
	v_lshlrev_b32_e32 v4, 3, v4
	v_cmp_gt_i32_e32 vcc, v4, v14
	v_lshlrev_b32_e32 v5, 3, v5
	s_mov_b32 s10, s6
	v_cndmask_b32_e32 v4, 25, v10, vcc
	v_cmp_gt_i32_e32 vcc, v5, v14
	s_waitcnt lgkmcnt(2)
	v_lshlrev_b32_e32 v5, 3, v6
	v_cndmask_b32_e32 v4, 26, v4, vcc
	v_cmp_gt_i32_e32 vcc, v5, v14
	v_lshlrev_b32_e32 v5, 3, v7
	v_bfe_u32 v7, v0, 2, 4
	v_cndmask_b32_e32 v4, 27, v4, vcc
	v_cmp_gt_i32_e32 vcc, v5, v14
	s_waitcnt lgkmcnt(1)
	v_lshlrev_b32_e32 v5, 3, v8
	v_and_or_b32 v10, v13, s13, v7
	v_cndmask_b32_e32 v4, 28, v4, vcc
	v_cmp_gt_i32_e32 vcc, v5, v14
	v_lshlrev_b32_e32 v5, 3, v9
	v_and_or_b32 v7, v12, 48, v7
	v_cndmask_b32_e32 v4, 29, v4, vcc
	v_cmp_gt_i32_e32 vcc, v5, v14
	s_waitcnt lgkmcnt(0)
	v_lshlrev_b32_e32 v5, 3, v11
	v_lshl_or_b32 v170, v7, 11, v3
	v_cndmask_b32_e32 v4, 30, v4, vcc
	v_cmp_gt_i32_e32 vcc, v5, v14
	v_lshl_or_b32 v171, v10, 11, v3
	v_or_b32_e32 v172, 0x40000, v170
	v_cndmask_b32_e32 v6, 31, v4, vcc
	v_lshlrev_b32_e32 v4, 2, v6
	v_add_u32_e32 v4, 0, v4
	v_add_u32_e32 v4, 0x27d00, v4
	ds_read2_b32 v[4:5], v4 offset1:1
	v_or_b32_e32 v173, 0x40000, v171
	v_readfirstlane_b32 s66, v6
	s_waitcnt lgkmcnt(0)
	v_sub_u32_e32 v5, v5, v4
	v_sub_u32_e32 v8, 0, v5
	v_max_i32_e32 v8, v5, v8
	v_cvt_f32_u32_e32 v9, v8
	v_lshlrev_b32_e32 v11, 3, v4
	v_sub_u32_e32 v11, v14, v11
	v_sub_u32_e32 v14, 0, v8
	v_rcp_iflag_f32_e32 v9, v9
	v_sub_u32_e32 v13, 0, v11
	v_max_i32_e32 v13, v11, v13
	v_xor_b32_e32 v12, v11, v5
	v_mul_f32_e32 v9, 0x4f7ffffe, v9
	v_cvt_u32_f32_e32 v9, v9
	v_ashrrev_i32_e32 v12, 31, v12
	v_mul_lo_u32 v14, v14, v9
	v_mul_hi_u32 v14, v9, v14
	v_add_u32_e32 v9, v9, v14
	v_mul_hi_u32 v9, v13, v9
	v_mul_lo_u32 v14, v9, v8
	v_sub_u32_e32 v13, v13, v14
	v_add_u32_e32 v14, 1, v9
	v_sub_u32_e32 v15, v13, v8
	v_cmp_ge_u32_e32 vcc, v13, v8
	s_nop 1
	v_cndmask_b32_e32 v9, v9, v14, vcc
	v_cndmask_b32_e32 v13, v13, v15, vcc
	v_add_u32_e32 v14, 1, v9
	v_cmp_ge_u32_e32 vcc, v13, v8
	s_nop 1
	v_cndmask_b32_e32 v8, v9, v14, vcc
	v_xor_b32_e32 v8, v8, v12
	v_sub_u32_e32 v8, v8, v12
	v_mul_lo_u32 v5, v8, v5
	v_sub_u32_e32 v5, v11, v5
	v_add_u32_e32 v4, v5, v4
	s_nop 0
	v_readfirstlane_b32 s62, v4
	v_lshlrev_b32_e32 v4, 3, v6
	v_add_u32_e32 v4, v8, v4
	s_lshl_b32 s69, s62, 19
	v_readfirstlane_b32 s65, v4
	s_lshl_b32 s70, s65, 19
	buffer_load_dwordx4 v163, s[8:11], s70 offen lds
	s_mov_b32 m0, s22
	s_or_b32 s12, s70, 0x40000
	buffer_load_dwordx4 v168, s[8:11], s70 offen lds
	s_mov_b32 m0, s24
	s_nop 0
	buffer_load_dwordx4 v163, s[8:11], s12 offen lds
	s_mov_b32 m0, s25
	s_nop 0
	buffer_load_dwordx4 v168, s[8:11], s12 offen lds
	s_mov_b32 m0, s20
	s_cmp_eq_u32 s16, 1
	buffer_load_dwordx4 v170, s[4:7], s69 offen lds
	s_mov_b32 m0, s23
	s_nop 0
	buffer_load_dwordx4 v171, s[4:7], s69 offen lds
	s_mov_b32 m0, s26
	s_cselect_b64 s[12:13], -1, 0
	buffer_load_dwordx4 v172, s[4:7], s69 offen lds
	s_mov_b32 m0, s27
	s_cmp_lg_u32 s16, 1
	buffer_load_dwordx4 v173, s[4:7], s69 offen lds
	v_readfirstlane_b32 s10, v5
	s_cbranch_scc1 .LBB0_999
	s_barrier
.LBB0_999:
	s_lshl_b32 s67, s10, 8
	s_add_u32 s14, s96, 0x4f800000
	s_addc_u32 s15, s97, 0
	s_add_i32 s28, s20, 0x18000
	s_or_b32 s17, s70, 0x80
	s_mov_b32 s10, s6
	s_mov_b32 s11, s7
	s_mov_b32 m0, s28
	s_add_i32 s29, s20, 0x1a000
	s_waitcnt vmcnt(2)
	s_barrier
	buffer_load_dwordx4 v163, s[8:11], s17 offen lds
	s_mov_b32 m0, s29
	s_add_i32 s30, s20, 0x8000
	buffer_load_dwordx4 v168, s[8:11], s17 offen lds
	s_or_b32 s17, s69, 0x80
	s_mov_b32 m0, s30
	s_add_i32 s31, s20, 0xa000
	buffer_load_dwordx4 v170, s[4:7], s17 offen lds
	s_mov_b32 m0, s31
	s_add_i32 s34, s20, 0x1c000
	buffer_load_dwordx4 v171, s[4:7], s17 offen lds
	s_or_b32 s17, s70, 0x40080
	s_mov_b32 m0, s34
	s_add_i32 s35, s20, 0x1e000
	buffer_load_dwordx4 v163, s[8:11], s17 offen lds
	s_mov_b32 m0, s35
	v_lshlrev_b32_e32 v3, 6, v0
	buffer_load_dwordx4 v168, s[8:11], s17 offen lds
	v_and_b32_e32 v3, 0x3c0, v3
	v_lshlrev_b32_e32 v4, 2, v0
	s_lshl_b32 s1, s1, 5
	v_lshl_or_b32 v3, v2, 1, v3
	s_lshl_b32 s10, s16, 13
	v_and_b32_e32 v4, 32, v4
	s_and_b32 s1, s1, 0x60
	v_mov_b32_e32 v18, 0
	v_bitop3_b32 v5, s10, v3, v4 bitop3:0xf6
	s_lshl_b32 s10, s1, 7
	s_waitcnt vmcnt(6)
	s_add_i32 s36, s20, 0xc000
	v_mov_b32_e32 v20, v18
	v_mov_b32_e32 v21, v18
	v_bitop3_b32 v3, s10, v3, v4 bitop3:0xf6
	s_cmpk_lt_u32 s0, 0x100
	v_mov_b32_e32 v19, v18
	v_mov_b64_e32 v[32:33], v[20:21]
	v_mov_b64_e32 v[24:25], v[20:21]
	v_mov_b64_e32 v[28:29], v[20:21]
	s_cselect_b64 s[16:17], -1, 0
	s_add_i32 s37, s20, 0xe000
	s_ashr_i32 s38, s94, 31
	v_ashrrev_i32_e32 v165, 31, v164
	v_or_b32_e32 v174, s1, v2
	s_mov_b32 s39, 0
	s_add_i32 s40, 0, 0x27d04
	s_add_i32 s41, 0, 0x27d0c
	s_add_i32 s42, 0, 0x27d14
	s_add_i32 s43, 0, 0x27d1c
	s_add_i32 s44, 0, 0x27d24
	s_add_i32 s45, 0, 0x27d2c
	s_add_i32 s46, 0, 0x27d34
	s_add_i32 s47, 0, 0x27d3c
	s_add_i32 s48, 0, 0x27d44
	s_add_i32 s49, 0, 0x27d4c
	s_add_i32 s50, 0, 0x27d54
	s_add_i32 s51, 0, 0x27d5c
	s_add_i32 s52, 0, 0x27d64
	s_add_i32 s53, 0, 0x27d6c
	s_add_i32 s56, 0, 0x27d74
	s_add_i32 s57, 0, 0x27d7c
	v_add_u32_e32 v175, 0, v3
	v_add_u32_e32 v176, 0, v5
	s_mov_b32 s18, 0x3c800000
	v_mov_b64_e32 v[30:31], v[18:19]
	v_mov_b64_e32 v[22:23], v[18:19]
	v_mov_b64_e32 v[26:27], v[18:19]
	s_barrier
	s_branch .LBB0_1002

; #define PG8_STAGE_A(bufoff, soff, voff) do { _Pragma("unroll") for (int _i = 0; _i < 2; ++_i) \
;         __builtin_amdgcn_raw_ptr_buffer_load_lds(rsA, (LAS void*)(lds + (bufoff) + ldsw + _i * 8192), 16, (voff)[_i], (soff), 0, 0); } while (0)
; #define PG8_STAGE_B(bufoff, soff) do { _Pragma("unroll") for (int _i = 0; _i < 2; ++_i) \
;         __builtin_amdgcn_raw_ptr_buffer_load_lds(rsB, (LAS void*)(lds + (bufoff) + ldsw + _i * 8192), 16, voffB[_i], (soff), 0, 0); } while (0)
; #define PG8_LDA(dst, b, h) do { _Pragma("unroll") for (int m = 0; m < 4; ++m) dst[m] = PG8_LD8(lds + PG8_SA(b, h) + aoff + m * 2048); } while (0)
; #define PG8_LDB(dst, b, h) do { _Pragma("unroll") for (int n = 0; n < 2; ++n) dst[n] = PG8_LD8(lds + PG8_SB(b, h) + boff + n * 2048); } while (0)
; #define PG8_WAIT_V(n) asm volatile("s_waitcnt vmcnt(" #n ")" ::: "memory")
; #define PG8_WAIT_L(n) asm volatile("s_waitcnt lgkmcnt(" #n ")" ::: "memory")
; #define PG8_BAR __builtin_amdgcn_s_barrier()
; #define PG8_SCHED __builtin_amdgcn_sched_barrier(0)
; template <class Epi, class Sched, bool GATHER, bool ALIGN_EPI, bool SP2, bool FP8>
; __device__ __forceinline__ void gemm_phase(LAS unsigned char* lds, const Gemm g, const Sched& S, const Epi& E) {
;     ...
;             PG8_LDB(B0, 0, 0); PG8_LDB(B1, 0, 1); PG8_SCHED; PG8_LDA(At, 0, 0); PG8_STAGE_A(PG8_SA(1, 1), a1, vA1);
;             PG8_WAIT_V(8); PG8_WAIT_L(0); PG8_BAR; PG8_MMA(0, 0, At, B0); PG8_MMA(0, 1, At, B1); PG8_BAR; PG8_SCHED;
;             PG8_LDA(At, 0, 1); PG8_STAGE_B(PG8_SB(0, 0), b2); PG8_STAGE_B(PG8_SB(0, 1), b2 + hstep); PG8_STAGE_A(PG8_SA(0, 0), a2, va20);
;             PG8_WAIT_V(8); PG8_WAIT_L(0); PG8_BAR; PG8_MMA(1, 0, At, B0); PG8_MMA(1, 1, At, B1); PG8_BAR; PG8_SCHED;
.LBB0_1005:
	s_add_i32 s74, s69, 0x80
	s_and_b64 s[72:73], s[10:11], exec
	s_cselect_b32 s74, s33, s74
	s_or_b32 s73, s74, 0x80
	s_and_b64 s[10:11], s[10:11], exec
	s_cselect_b32 s72, s68, s70
	s_mov_b32 s10, s6
	s_mov_b32 s11, s7
	v_add_u32_e32 v14, 0x10000, v175
	ds_read_b128 v[2:5], v14
	ds_read_b128 v[6:9], v14 offset:1024
	ds_read_b128 v[10:13], v14 offset:2048
	ds_read_b128 v[14:17], v14 offset:3072
	v_add_u32_e32 v177, 0x14000, v175
	ds_read_b128 v[210:213], v177
	ds_read_b128 v[214:217], v177 offset:1024
	ds_read_b128 v[218:221], v177 offset:2048
	ds_read_b128 v[222:225], v177 offset:3072
	ds_read_b128 v[178:181], v176
	ds_read_b128 v[182:185], v176 offset:1024
	ds_read_b128 v[186:189], v176 offset:2048
	ds_read_b128 v[190:193], v176 offset:3072
	ds_read_b128 v[194:197], v176 offset:4096
	ds_read_b128 v[198:201], v176 offset:5120
	ds_read_b128 v[202:205], v176 offset:6144
	ds_read_b128 v[206:209], v176 offset:7168
	s_mov_b32 m0, s36
	s_nop 0
	buffer_load_dwordx4 v172, s[4:7], s69 offen lds
	s_mov_b32 m0, s37
	s_nop 0
	buffer_load_dwordx4 v173, s[4:7], s69 offen lds
	s_waitcnt vmcnt(8)
	s_waitcnt lgkmcnt(0)
	s_barrier
	s_setprio 1
	v_mfma_f32_16x16x128_f8f6f4 v[158:161], v[2:9], v[178:185], v[158:161]
	v_mfma_f32_16x16x128_f8f6f4 v[154:157], v[10:17], v[178:185], v[154:157]
	v_mfma_f32_16x16x128_f8f6f4 v[142:145], v[2:9], v[186:193], v[142:145]
	v_mfma_f32_16x16x128_f8f6f4 v[138:141], v[10:17], v[186:193], v[138:141]
	v_mfma_f32_16x16x128_f8f6f4 v[126:129], v[2:9], v[194:201], v[126:129]
	v_mfma_f32_16x16x128_f8f6f4 v[122:125], v[10:17], v[194:201], v[122:125]
	v_mfma_f32_16x16x128_f8f6f4 v[110:113], v[2:9], v[202:209], v[110:113]
	v_mfma_f32_16x16x128_f8f6f4 v[106:109], v[10:17], v[202:209], v[106:109]
	v_mfma_f32_16x16x128_f8f6f4 v[150:153], v[210:217], v[178:185], v[150:153]
	v_mfma_f32_16x16x128_f8f6f4 v[146:149], v[218:225], v[178:185], v[146:149]
	v_mfma_f32_16x16x128_f8f6f4 v[134:137], v[210:217], v[186:193], v[134:137]
	v_mfma_f32_16x16x128_f8f6f4 v[130:133], v[218:225], v[186:193], v[130:133]
	v_mfma_f32_16x16x128_f8f6f4 v[118:121], v[210:217], v[194:201], v[118:121]
	v_mfma_f32_16x16x128_f8f6f4 v[114:117], v[218:225], v[194:201], v[114:117]
	v_mfma_f32_16x16x128_f8f6f4 v[102:105], v[210:217], v[202:209], v[102:105]
	v_mfma_f32_16x16x128_f8f6f4 v[98:101], v[218:225], v[202:209], v[98:101]
	s_setprio 0
	s_barrier
	ds_read_b128 v[178:181], v176 offset:16384
	ds_read_b128 v[182:185], v176 offset:17408
	ds_read_b128 v[186:189], v176 offset:18432
	ds_read_b128 v[190:193], v176 offset:19456
	ds_read_b128 v[194:197], v176 offset:20480
	ds_read_b128 v[198:201], v176 offset:21504
	ds_read_b128 v[202:205], v176 offset:22528
	ds_read_b128 v[206:209], v176 offset:23552
	s_mov_b32 m0, s21
	s_nop 0
	buffer_load_dwordx4 v163, s[8:11], s72 offen lds
	s_mov_b32 m0, s22
	s_nop 0
	buffer_load_dwordx4 v168, s[8:11], s72 offen lds
	s_add_i32 s75, s72, 0x40000
	s_mov_b32 m0, s24
	s_nop 0
	buffer_load_dwordx4 v163, s[8:11], s75 offen lds
	s_mov_b32 m0, s25
	s_nop 0
	buffer_load_dwordx4 v168, s[8:11], s75 offen lds
	s_mov_b32 m0, s20
	s_nop 0
	buffer_load_dwordx4 v170, s[4:7], s74 offen lds
	s_mov_b32 m0, s23
	s_nop 0
	buffer_load_dwordx4 v171, s[4:7], s74 offen lds
	s_waitcnt vmcnt(8)
	s_waitcnt lgkmcnt(0)
	s_barrier
	s_setprio 1
	v_mfma_f32_16x16x128_f8f6f4 v[94:97], v[2:9], v[178:185], v[94:97]
	v_mfma_f32_16x16x128_f8f6f4 v[90:93], v[10:17], v[178:185], v[90:93]
	v_mfma_f32_16x16x128_f8f6f4 v[78:81], v[2:9], v[186:193], v[78:81]
	v_mfma_f32_16x16x128_f8f6f4 v[74:77], v[10:17], v[186:193], v[74:77]
	v_mfma_f32_16x16x128_f8f6f4 v[62:65], v[2:9], v[194:201], v[62:65]
	v_mfma_f32_16x16x128_f8f6f4 v[58:61], v[10:17], v[194:201], v[58:61]
	v_mfma_f32_16x16x128_f8f6f4 v[46:49], v[2:9], v[202:209], v[46:49]
	v_mfma_f32_16x16x128_f8f6f4 v[42:45], v[10:17], v[202:209], v[42:45]
	v_mfma_f32_16x16x128_f8f6f4 v[86:89], v[210:217], v[178:185], v[86:89]
	v_mfma_f32_16x16x128_f8f6f4 v[82:85], v[218:225], v[178:185], v[82:85]
	v_mfma_f32_16x16x128_f8f6f4 v[70:73], v[210:217], v[186:193], v[70:73]
	v_mfma_f32_16x16x128_f8f6f4 v[66:69], v[218:225], v[186:193], v[66:69]
	v_mfma_f32_16x16x128_f8f6f4 v[54:57], v[210:217], v[194:201], v[54:57]
	v_mfma_f32_16x16x128_f8f6f4 v[50:53], v[218:225], v[194:201], v[50:53]
	v_mfma_f32_16x16x128_f8f6f4 v[38:41], v[210:217], v[202:209], v[38:41]
	v_mfma_f32_16x16x128_f8f6f4 v[34:37], v[218:225], v[202:209], v[34:37]
	s_setprio 0
	s_barrier
; #define PG8_STAGE_A(bufoff, soff, voff) do { _Pragma("unroll") for (int _i = 0; _i < 2; ++_i) \
;         __builtin_amdgcn_raw_ptr_buffer_load_lds(rsA, (LAS void*)(lds + (bufoff) + ldsw + _i * 8192), 16, (voff)[_i], (soff), 0, 0); } while (0)
; #define PG8_STAGE_B(bufoff, soff) do { _Pragma("unroll") for (int _i = 0; _i < 2; ++_i) \
;         __builtin_amdgcn_raw_ptr_buffer_load_lds(rsB, (LAS void*)(lds + (bufoff) + ldsw + _i * 8192), 16, voffB[_i], (soff), 0, 0); } while (0)
; #define PG8_LDA(dst, b, h) do { _Pragma("unroll") for (int m = 0; m < 4; ++m) dst[m] = PG8_LD8(lds + PG8_SA(b, h) + aoff + m * 2048); } while (0)
; #define PG8_LDB(dst, b, h) do { _Pragma("unroll") for (int n = 0; n < 2; ++n) dst[n] = PG8_LD8(lds + PG8_SB(b, h) + boff + n * 2048); } while (0)
; #define PG8_WAIT_V(n) asm volatile("s_waitcnt vmcnt(" #n ")" ::: "memory")
; #define PG8_WAIT_L(n) asm volatile("s_waitcnt lgkmcnt(" #n ")" ::: "memory")
; #define PG8_BAR __builtin_amdgcn_s_barrier()
; #define PG8_SCHED __builtin_amdgcn_sched_barrier(0)
; template <class Epi, class Sched, bool GATHER, bool ALIGN_EPI, bool SP2, bool FP8>
; __device__ __forceinline__ void gemm_phase(LAS unsigned char* lds, const Gemm g, const Sched& S, const Epi& E) {
;     ...
;             PG8_LDB(B0, 1, 0); PG8_LDB(B1, 1, 1); PG8_SCHED; PG8_LDA(At, 1, 0); PG8_STAGE_A(PG8_SA(0, 1), a2, va21);
;             PG8_WAIT_V(8); PG8_WAIT_L(0); PG8_BAR; PG8_MMA(0, 0, At, B0); PG8_MMA(0, 1, At, B1); PG8_BAR; PG8_SCHED;
;             PG8_LDA(At, 1, 1); PG8_STAGE_B(PG8_SB(1, 0), b3); PG8_STAGE_B(PG8_SB(1, 1), b3 + hstep); PG8_STAGE_A(PG8_SA(1, 0), a3, va20);
;             PG8_WAIT_V(8); PG8_WAIT_L(0); PG8_BAR; PG8_MMA(1, 0, At, B0); PG8_MMA(1, 1, At, B1); PG8_BAR; PG8_SCHED;
	v_add_u32_e32 v14, 0x18000, v175
	ds_read_b128 v[2:5], v14
	ds_read_b128 v[6:9], v14 offset:1024
	ds_read_b128 v[10:13], v14 offset:2048
	ds_read_b128 v[14:17], v14 offset:3072
	v_add_u32_e32 v177, 0x1c000, v175
	ds_read_b128 v[210:213], v177
	ds_read_b128 v[214:217], v177 offset:1024
	ds_read_b128 v[218:221], v177 offset:2048
	ds_read_b128 v[222:225], v177 offset:3072
	ds_read_b128 v[178:181], v176 offset:32768
	ds_read_b128 v[182:185], v176 offset:33792
	ds_read_b128 v[186:189], v176 offset:34816
	ds_read_b128 v[190:193], v176 offset:35840
	ds_read_b128 v[194:197], v176 offset:36864
	ds_read_b128 v[198:201], v176 offset:37888
	ds_read_b128 v[202:205], v176 offset:38912
	ds_read_b128 v[206:209], v176 offset:39936
	s_mov_b32 m0, s26
	s_nop 0
	buffer_load_dwordx4 v172, s[4:7], s74 offen lds
	s_mov_b32 m0, s27
	s_nop 0
	buffer_load_dwordx4 v173, s[4:7], s74 offen lds
	s_waitcnt vmcnt(8)
	s_waitcnt lgkmcnt(0)
	s_barrier
	s_setprio 1
	v_mfma_f32_16x16x128_f8f6f4 v[158:161], v[2:9], v[178:185], v[158:161]
	v_mfma_f32_16x16x128_f8f6f4 v[154:157], v[10:17], v[178:185], v[154:157]
	v_mfma_f32_16x16x128_f8f6f4 v[142:145], v[2:9], v[186:193], v[142:145]
	v_mfma_f32_16x16x128_f8f6f4 v[138:141], v[10:17], v[186:193], v[138:141]
	v_mfma_f32_16x16x128_f8f6f4 v[126:129], v[2:9], v[194:201], v[126:129]
	v_mfma_f32_16x16x128_f8f6f4 v[122:125], v[10:17], v[194:201], v[122:125]
	v_mfma_f32_16x16x128_f8f6f4 v[110:113], v[2:9], v[202:209], v[110:113]
	v_mfma_f32_16x16x128_f8f6f4 v[106:109], v[10:17], v[202:209], v[106:109]
	v_mfma_f32_16x16x128_f8f6f4 v[150:153], v[210:217], v[178:185], v[150:153]
	v_mfma_f32_16x16x128_f8f6f4 v[146:149], v[218:225], v[178:185], v[146:149]
	v_mfma_f32_16x16x128_f8f6f4 v[134:137], v[210:217], v[186:193], v[134:137]
	v_mfma_f32_16x16x128_f8f6f4 v[130:133], v[218:225], v[186:193], v[130:133]
	v_mfma_f32_16x16x128_f8f6f4 v[118:121], v[210:217], v[194:201], v[118:121]
	v_mfma_f32_16x16x128_f8f6f4 v[114:117], v[218:225], v[194:201], v[114:117]
	v_mfma_f32_16x16x128_f8f6f4 v[102:105], v[210:217], v[202:209], v[102:105]
	v_mfma_f32_16x16x128_f8f6f4 v[98:101], v[218:225], v[202:209], v[98:101]
	s_setprio 0
	s_barrier
	ds_read_b128 v[178:181], v176 offset:49152
	ds_read_b128 v[182:185], v176 offset:50176
	ds_read_b128 v[186:189], v176 offset:51200
	ds_read_b128 v[190:193], v176 offset:52224
	ds_read_b128 v[194:197], v176 offset:53248
	ds_read_b128 v[198:201], v176 offset:54272
	ds_read_b128 v[202:205], v176 offset:55296
	ds_read_b128 v[206:209], v176 offset:56320
	s_or_b32 s72, s72, 0x80
	s_mov_b32 m0, s28
	s_nop 0
	buffer_load_dwordx4 v163, s[8:11], s72 offen lds
	s_mov_b32 m0, s29
	s_nop 0
	buffer_load_dwordx4 v168, s[8:11], s72 offen lds
	s_add_i32 s75, s72, 0x40000
	s_mov_b32 m0, s34
	s_nop 0
	buffer_load_dwordx4 v163, s[8:11], s75 offen lds
	s_mov_b32 m0, s35
	s_nop 0
	buffer_load_dwordx4 v168, s[8:11], s75 offen lds
	s_mov_b32 m0, s30
	s_nop 0
	buffer_load_dwordx4 v170, s[4:7], s73 offen lds
	s_mov_b32 m0, s31
	s_nop 0
	buffer_load_dwordx4 v171, s[4:7], s73 offen lds
	s_waitcnt vmcnt(8)
	s_waitcnt lgkmcnt(0)
	s_barrier
	s_setprio 1
	v_mfma_f32_16x16x128_f8f6f4 v[94:97], v[2:9], v[178:185], v[94:97]
	v_mfma_f32_16x16x128_f8f6f4 v[90:93], v[10:17], v[178:185], v[90:93]
	v_mfma_f32_16x16x128_f8f6f4 v[78:81], v[2:9], v[186:193], v[78:81]
	v_mfma_f32_16x16x128_f8f6f4 v[74:77], v[10:17], v[186:193], v[74:77]
	v_mfma_f32_16x16x128_f8f6f4 v[62:65], v[2:9], v[194:201], v[62:65]
	v_mfma_f32_16x16x128_f8f6f4 v[58:61], v[10:17], v[194:201], v[58:61]
	v_mfma_f32_16x16x128_f8f6f4 v[46:49], v[2:9], v[202:209], v[46:49]
	v_mfma_f32_16x16x128_f8f6f4 v[42:45], v[10:17], v[202:209], v[42:45]
	v_mfma_f32_16x16x128_f8f6f4 v[86:89], v[210:217], v[178:185], v[86:89]
	v_mfma_f32_16x16x128_f8f6f4 v[82:85], v[218:225], v[178:185], v[82:85]
	v_mfma_f32_16x16x128_f8f6f4 v[70:73], v[210:217], v[186:193], v[70:73]
	v_mfma_f32_16x16x128_f8f6f4 v[66:69], v[218:225], v[186:193], v[66:69]
	v_mfma_f32_16x16x128_f8f6f4 v[54:57], v[210:217], v[194:201], v[54:57]
	v_mfma_f32_16x16x128_f8f6f4 v[50:53], v[218:225], v[194:201], v[50:53]
	v_mfma_f32_16x16x128_f8f6f4 v[38:41], v[210:217], v[202:209], v[38:41]
	v_mfma_f32_16x16x128_f8f6f4 v[34:37], v[218:225], v[202:209], v[34:37]
	s_setprio 0
	s_add_i32 s71, s71, 2
	s_addk_i32 s69, 0x100
	s_addk_i32 s70, 0x100
	s_cmp_gt_u32 s71, 13
	s_barrier
	s_cbranch_scc1 .LBB0_1008
